# speedup vs baseline: 1.0013x; 1.0013x over previous
.LBB2_13:
	v_exp_f32_e32 v48, v48
	v_exp_f32_e32 v49, v49
	v_mfma_f32_32x32x16_bf16 v[112:127], a[192:195], a[128:131], v[16:31]
	ds_read_b64_tr_b16 v[180:181], v223 offset:0
	v_cvt_pk_bf16_f32 v164, v128, v129
	v_exp_f32_e32 v50, v50
	v_exp_f32_e32 v51, v51
	v_mfma_f32_32x32x16_bf16 v[96:111], a[192:195], a[160:163], v[0:15]
	ds_read_b64_tr_b16 v[182:183], v223 offset:0x800
	v_cvt_pk_bf16_f32 v165, v130, v131
	v_mfma_f32_32x32x16_bf16 v[80:95], a[224:227], a[128:131], v[16:31]
	ds_read_b64_tr_b16 v[184:185], v223 offset:0x200
	v_exp_f32_e32 v236, v52
	v_exp_f32_e32 v237, v53
	v_cvt_pk_bf16_f32 v166, v132, v133
	v_mfma_f32_32x32x16_bf16 v[64:79], a[224:227], a[160:163], v[0:15]
	ds_read_b64_tr_b16 v[186:187], v223 offset:0xa00
	ds_read_b64_tr_b16 v[176:177], v223 offset:0x400
	v_exp_f32_e32 v242, v54
	v_exp_f32_e32 v243, v55
	v_cvt_pk_bf16_f32 v167, v134, v135
	v_exp_f32_e32 v198, v56
	v_exp_f32_e32 v199, v57
	v_mfma_f32_32x32x16_bf16 v[112:127], a[196:199], a[132:135], v[112:127]
	ds_read_b64_tr_b16 v[178:179], v223 offset:0xc00
	v_cvt_pk_bf16_f32 v128, v136, v137
	v_exp_f32_e32 v230, v58
	v_exp_f32_e32 v231, v59
	v_mfma_f32_32x32x16_bf16 v[96:111], a[196:199], a[164:167], v[96:111]
	ds_read_b64_tr_b16 v[188:189], v223 offset:0x600
	v_cvt_pk_bf16_f32 v129, v138, v139
	v_exp_f32_e32 v232, v60
	v_exp_f32_e32 v233, v61
	v_mfma_f32_32x32x16_bf16 v[80:95], a[228:231], a[132:135], v[80:95]
	ds_read_b64_tr_b16 v[190:191], v223 offset:0xe00
	v_cvt_pk_bf16_f32 v130, v140, v141
	v_mfma_f32_32x32x16_bf16 v[64:79], a[228:231], a[164:167], v[64:79]
	ds_read_b64_tr_b16 v[172:173], v223 offset:0x1000
	v_exp_f32_e32 v234, v62
	v_exp_f32_e32 v235, v63
	ds_read_b64_tr_b16 v[174:175], v223 offset:0x1800
	v_cvt_pk_bf16_f32 v131, v142, v143
	v_exp_f32_e32 v141, v32
	v_exp_f32_e32 v142, v33
	v_mfma_f32_32x32x16_bf16 v[112:127], a[200:203], a[136:139], v[112:127]
	ds_read_b64_tr_b16 v[168:169], v223 offset:0x1200
	v_cvt_pk_bf16_f32 v192, v144, v145
	v_exp_f32_e32 v143, v34
	v_mfma_f32_32x32x16_bf16 v[96:111], a[200:203], a[168:171], v[96:111]
	ds_read_b64_tr_b16 v[170:171], v223 offset:0x1a00
	v_exp_f32_e32 v244, v35
	v_cvt_pk_bf16_f32 v193, v146, v147
	v_mfma_f32_32x32x16_bf16 v[80:95], a[232:235], a[136:139], v[80:95]
	ds_read_b64_tr_b16 v[160:161], v223 offset:0x1400
	v_exp_f32_e32 v245, v36
	v_exp_f32_e32 v246, v37
	v_cvt_pk_bf16_f32 v194, v148, v149
	v_mfma_f32_32x32x16_bf16 v[64:79], a[232:235], a[168:171], v[64:79]
	ds_read_b64_tr_b16 v[162:163], v223 offset:0x1c00
	ds_read_b64_tr_b16 v[136:137], v223 offset:0x1600
	v_exp_f32_e32 v247, v38
	v_exp_f32_e32 v248, v39
	v_cvt_pk_bf16_f32 v195, v150, v151
	v_exp_f32_e32 v148, v40
	v_exp_f32_e32 v149, v41
	v_mfma_f32_32x32x16_bf16 v[112:127], a[204:207], a[140:143], v[112:127]
	ds_read_b64_tr_b16 v[138:139], v223 offset:0x1e00
	v_cvt_pk_bf16_f32 v144, v152, v153
	v_exp_f32_e32 v150, v42
	v_exp_f32_e32 v151, v43
	v_mfma_f32_32x32x16_bf16 v[96:111], a[204:207], a[172:175], v[96:111]
	ds_read_b64_tr_b16 v[132:133], v223 offset:0x2000
	v_cvt_pk_bf16_f32 v145, v154, v155
	v_exp_f32_e32 v152, v44
	v_exp_f32_e32 v153, v45
	v_mfma_f32_32x32x16_bf16 v[80:95], a[236:239], a[140:143], v[80:95]
	ds_read_b64_tr_b16 v[134:135], v223 offset:0x2800
	v_cvt_pk_bf16_f32 v146, v156, v157
	v_mfma_f32_32x32x16_bf16 v[64:79], a[236:239], a[172:175], v[64:79]
	ds_read_b64_tr_b16 v[60:61], v223 offset:0x2200
	v_exp_f32_e32 v154, v46
	v_exp_f32_e32 v155, v47
	ds_read_b64_tr_b16 v[62:63], v223 offset:0x2a00
	v_cvt_pk_bf16_f32 v147, v158, v159
	s_mov_b32 s0, s30
	v_mfma_f32_32x32x16_bf16 v[112:127], a[208:211], a[144:147], v[112:127]
	ds_read_b64_tr_b16 v[56:57], v223 offset:0x2400
	v_cvt_pk_bf16_f32 v52, v48, v49
	v_add_f32_e32 v32, v239, v48
	v_add_f32_e32 v33, v238, v49
	s_add_i32 s19, s17, 0xfffda000
	s_mov_b32 s1, s19
	v_mfma_f32_32x32x16_bf16 v[96:111], a[208:211], a[176:179], v[96:111]
	ds_read_b64_tr_b16 v[58:59], v223 offset:0x2c00
	v_cvt_pk_bf16_f32 v53, v50, v51
	v_add_f32_e32 v32, v32, v50
	v_add_f32_e32 v33, v33, v51
	s_mov_b32 s81, s37
	v_mfma_f32_32x32x16_bf16 v[80:95], a[240:243], a[144:147], v[80:95]
	ds_read_b64_tr_b16 v[48:49], v223 offset:0x2600
	v_cvt_pk_bf16_f32 v54, v236, v237
	v_add_f32_e32 v32, v32, v236
	v_add_f32_e32 v33, v33, v237
	s_add_i32 s82, s17, 0xfffdc000
	v_mfma_f32_32x32x16_bf16 v[64:79], a[240:243], a[176:179], v[64:79]
	ds_read_b64_tr_b16 v[50:51], v223 offset:0x2e00
	ds_read_b64_tr_b16 v[44:45], v223 offset:0x3000
	v_cvt_pk_bf16_f32 v55, v242, v243
	v_add_f32_e32 v32, v32, v242
	v_add_f32_e32 v33, v33, v243
	s_mov_b32 s83, s39
	v_mfma_f32_32x32x16_bf16 v[112:127], a[212:215], a[148:151], v[112:127]
	ds_read_b64_tr_b16 v[46:47], v223 offset:0x3800
	v_add_f32_e32 v32, v32, v198
	v_add_f32_e32 v33, v33, v199
	s_add_i32 s24, s17, 0xfffde000
	s_mov_b32 s84, s24
	v_mfma_f32_32x32x16_bf16 v[96:111], a[212:215], a[180:183], v[96:111]
	ds_read_b64_tr_b16 v[40:41], v223 offset:0x3200
	v_add_f32_e32 v32, v32, v230
	v_add_f32_e32 v33, v33, v231
	s_mov_b32 s85, s41
	v_mfma_f32_32x32x16_bf16 v[80:95], a[244:247], a[148:151], v[80:95]
	ds_read_b64_tr_b16 v[42:43], v223 offset:0x3a00
	v_add_f32_e32 v32, v32, v232
	v_add_f32_e32 v33, v33, v233
	s_add_i32 s86, s17, 0xfffe0000
	v_mfma_f32_32x32x16_bf16 v[64:79], a[244:247], a[180:183], v[64:79]
	ds_read_b64_tr_b16 v[36:37], v223 offset:0x3400
	ds_read_b64_tr_b16 v[38:39], v223 offset:0x3c00
	v_add_f32_e32 v156, v32, v234
	v_add_f32_e32 v157, v33, v235
	s_mov_b32 s87, s43
	v_mfma_f32_32x32x16_bf16 v[112:127], a[216:219], a[152:155], v[112:127]
	ds_read_b64_tr_b16 v[32:33], v223 offset:0x3600
	v_cvt_pk_bf16_f32 v140, v141, v142
	v_add_f32_e32 v158, v240, v141
	v_add_f32_e32 v142, v241, v142
	s_add_i32 s88, s17, 0xfffba000
	v_mfma_f32_32x32x16_bf16 v[96:111], a[216:219], a[184:187], v[96:111]
	ds_read_b64_tr_b16 v[34:35], v223 offset:0x3e00
	v_cvt_pk_bf16_f32 v141, v143, v244
	v_add_f32_e32 v143, v158, v143
	v_add_f32_e32 v158, v142, v244
	v_mfma_f32_32x32x16_bf16 v[80:95], a[248:251], a[152:155], v[80:95]
	s_mov_b32 s89, s45
	v_cvt_pk_bf16_f32 v142, v245, v246
	v_add_f32_e32 v159, v143, v245
	v_add_f32_e32 v158, v158, v246
	v_mfma_f32_32x32x16_bf16 v[64:79], a[248:251], a[184:187], v[64:79]
	s_add_i32 s90, s17, 0xfffba080
	v_cvt_pk_bf16_f32 v143, v247, v248
	v_add_f32_e32 v159, v159, v247
	v_add_f32_e32 v158, v158, v248
	v_mfma_f32_32x32x16_bf16 v[112:127], a[220:223], a[156:159], v[112:127]
	s_mov_b32 s91, s47
	v_add_f32_e32 v159, v159, v148
	v_add_f32_e32 v158, v158, v149
	v_mfma_f32_32x32x16_bf16 v[96:111], a[220:223], a[188:191], v[96:111]
	s_add_i32 s92, s17, 0xfffbe000
	v_add_f32_e32 v159, v159, v150
	v_add_f32_e32 v158, v158, v151
	v_mfma_f32_32x32x16_bf16 v[80:95], a[252:255], a[156:159], v[80:95]
	s_mov_b32 s93, s49
	v_add_f32_e32 v159, v159, v152
	v_add_f32_e32 v158, v158, v153
	v_mfma_f32_32x32x16_bf16 v[64:79], a[252:255], a[188:191], v[64:79]
	s_add_i32 s94, s17, 0xfffbe080
	v_add_f32_e32 v159, v159, v154
	v_add_f32_e32 v158, v158, v155
	s_nop 4
	v_add_f32_e32 v156, v156, v157
	s_waitcnt vmcnt(0) lgkmcnt(0)
	s_barrier
	s_nop 0
	v_mov_b32_e32 v157, v156
	s_nop 1
	v_permlane32_swap_b32_e32 v156, v157
	v_add_f32_e32 v156, v156, v157
	v_add_f32_e32 v197, v197, v156
	v_add_f32_e32 v156, v159, v158
	v_mov_b32_e32 v157, v156
	s_nop 1
	v_permlane32_swap_b32_e32 v156, v157
	v_add_f32_e32 v156, v156, v157
	v_add_f32_e32 v196, v196, v156
	s_nop 1
	s_mov_b32 m0, s0
	v_mfma_f32_32x32x16_bf16 a[0:15], v[180:183], v[164:167], a[0:15]
	buffer_load_dwordx4 v209, s[4:7], s1 offen lds
	s_mov_b32 m0, s81
	v_mfma_f32_32x32x16_bf16 a[16:31], v[180:183], v[192:195], a[16:31]
	buffer_load_dwordx4 v210, s[4:7], s82 offen lds
	ds_read_b128 a[192:195], v219 offset:0
	s_mov_b32 m0, s83
	v_mfma_f32_32x32x16_bf16 a[32:47], v[184:187], v[164:167], a[32:47]
	buffer_load_dwordx4 v209, s[4:7], s84 offen lds
	ds_read_b128 a[196:199], v220 offset:0
	s_mov_b32 m0, s85
	v_mfma_f32_32x32x16_bf16 a[48:63], v[184:187], v[192:195], a[48:63]
	buffer_load_dwordx4 v210, s[4:7], s86 offen lds
	ds_read_b128 a[200:203], v221 offset:0
	s_mov_b32 m0, s87
	v_mfma_f32_32x32x16_bf16 a[64:79], v[176:179], v[164:167], a[64:79]
	buffer_load_dwordx4 v211, s[20:23], s88 offen lds
	ds_read_b128 a[204:207], v222 offset:0
	s_mov_b32 m0, s89
	v_mfma_f32_32x32x16_bf16 a[80:95], v[176:179], v[192:195], a[80:95]
	buffer_load_dwordx4 v211, s[20:23], s90 offen lds
	ds_read_b128 a[208:211], v219 offset:128
	s_mov_b32 m0, s91
	v_mfma_f32_32x32x16_bf16 a[96:111], v[188:191], v[164:167], a[96:111]
	buffer_load_dwordx4 v211, s[20:23], s92 offen lds
	ds_read_b128 a[212:215], v220 offset:128
	s_mov_b32 m0, s93
	v_mfma_f32_32x32x16_bf16 a[112:127], v[188:191], v[192:195], a[112:127]
	buffer_load_dwordx4 v211, s[20:23], s94 offen lds
	ds_read_b128 a[216:219], v221 offset:128
	v_mfma_f32_32x32x16_bf16 a[0:15], v[172:175], v[128:131], a[0:15]
	ds_read_b128 a[220:223], v222 offset:128
	v_max3_f32 v156, v112, v113, v80
	v_max3_f32 v157, v114, v115, v81
	v_max3_f32 v156, v156, v82, v83
	v_mfma_f32_32x32x16_bf16 a[16:31], v[172:175], v[144:147], a[16:31]
	ds_read_b128 a[224:227], v219 offset:8192
	v_max3_f32 v156, v156, v116, v117
	v_max3_f32 v157, v157, v118, v119
	v_max3_f32 v156, v156, v84, v85
	v_max3_f32 v157, v157, v86, v87
	v_mfma_f32_32x32x16_bf16 a[32:47], v[168:171], v[128:131], a[32:47]
	ds_read_b128 a[228:231], v220 offset:8192
	v_max3_f32 v156, v156, v120, v121
	v_max3_f32 v157, v157, v122, v123
	v_max3_f32 v156, v156, v88, v89
	v_max3_f32 v157, v157, v90, v91
	v_mfma_f32_32x32x16_bf16 a[48:63], v[168:171], v[144:147], a[48:63]
	ds_read_b128 a[232:235], v221 offset:8192
	v_max3_f32 v156, v156, v124, v125
	v_max3_f32 v157, v157, v126, v127
	v_max3_f32 v156, v156, v92, v93
	v_max3_f32 v157, v157, v94, v95
	v_mfma_f32_32x32x16_bf16 a[64:79], v[160:163], v[128:131], a[64:79]
	ds_read_b128 a[236:239], v222 offset:8192
	v_max3_f32 v158, v96, v97, v64
	v_max3_f32 v159, v98, v99, v65
	v_max3_f32 v158, v158, v66, v67
	v_mfma_f32_32x32x16_bf16 a[80:95], v[160:163], v[144:147], a[80:95]
	ds_read_b128 a[240:243], v219 offset:8320
	v_max3_f32 v158, v158, v100, v101
	v_max3_f32 v159, v159, v102, v103
	v_max3_f32 v158, v158, v68, v69
	v_max3_f32 v159, v159, v70, v71
	v_mfma_f32_32x32x16_bf16 a[96:111], v[136:139], v[128:131], a[96:111]
	ds_read_b128 a[244:247], v220 offset:8320
	v_max3_f32 v128, v158, v104, v105
	v_max3_f32 v129, v159, v106, v107
	v_max3_f32 v128, v128, v72, v73
	v_max3_f32 v129, v129, v74, v75
	v_mfma_f32_32x32x16_bf16 a[112:127], v[136:139], v[144:147], a[112:127]
	ds_read_b128 a[248:251], v221 offset:8320
	v_max3_f32 v128, v128, v108, v109
	v_max3_f32 v129, v129, v110, v111
	v_max3_f32 v128, v128, v76, v77
	v_max3_f32 v130, v129, v78, v79
	v_mfma_f32_32x32x16_bf16 a[0:15], v[132:135], v[52:55], a[0:15]
	ds_read_b128 a[252:255], v222 offset:8320
	v_max_f32_e32 v129, v156, v157
	v_mov_b32_e32 v131, v129
	s_nop 1
	v_permlane32_swap_b32_e32 v129, v131
	v_max_f32_e32 v129, v129, v131
	v_mfma_f32_32x32x16_bf16 a[16:31], v[132:135], v[140:143], a[16:31]
	v_max_f32_e32 v128, v128, v130
	v_mov_b32_e32 v130, v128
	s_nop 1
	v_permlane32_swap_b32_e32 v128, v130
	v_max_f32_e32 v128, v128, v130
	v_max_f32_e32 v130, v129, v129
	v_max_f32_e32 v131, v128, v128
	v_max_f32_e32 v130, v130, v131
	v_mfma_f32_32x32x16_bf16 a[32:47], v[60:63], v[52:55], a[32:47]
	v_cmp_lt_f32_e32 vcc, s79, v130
	s_cmp_lg_u64 vcc, 0
	s_cselect_b64 s[0:1], -1, 0
	s_cbranch_vccnz .LBB2_18

.LBB2_15:
	s_waitcnt lgkmcnt(0)
	v_exp_f32_e32 v80, v80
	v_exp_f32_e32 v81, v81
	v_mfma_f32_32x32x16_bf16 v[112:127], a[192:195], a[128:131], v[16:31]
	ds_read_b64_tr_b16 v[180:181], v208 offset:0
	v_cvt_pk_bf16_f32 v164, v128, v129
	v_exp_f32_e32 v82, v82
	v_exp_f32_e32 v83, v83
	v_mfma_f32_32x32x16_bf16 v[96:111], a[192:195], a[160:163], v[0:15]
	ds_read_b64_tr_b16 v[182:183], v208 offset:0x800
	v_cvt_pk_bf16_f32 v165, v130, v131
	v_mfma_f32_32x32x16_bf16 v[48:63], a[224:227], a[128:131], v[16:31]
	ds_read_b64_tr_b16 v[184:185], v208 offset:0x200
	v_exp_f32_e32 v240, v84
	v_exp_f32_e32 v241, v85
	v_cvt_pk_bf16_f32 v166, v132, v133
	v_mfma_f32_32x32x16_bf16 v[32:47], a[224:227], a[160:163], v[0:15]
	ds_read_b64_tr_b16 v[186:187], v208 offset:0xa00
	ds_read_b64_tr_b16 v[176:177], v208 offset:0x400
	v_exp_f32_e32 v242, v86
	v_exp_f32_e32 v243, v87
	v_cvt_pk_bf16_f32 v167, v134, v135
	v_exp_f32_e32 v198, v88
	v_exp_f32_e32 v199, v89
	v_mfma_f32_32x32x16_bf16 v[112:127], a[196:199], a[132:135], v[112:127]
	ds_read_b64_tr_b16 v[178:179], v208 offset:0xc00
	v_cvt_pk_bf16_f32 v128, v136, v137
	v_exp_f32_e32 v230, v90
	v_exp_f32_e32 v231, v91
	v_mfma_f32_32x32x16_bf16 v[96:111], a[196:199], a[164:167], v[96:111]
	ds_read_b64_tr_b16 v[188:189], v208 offset:0x600
	v_cvt_pk_bf16_f32 v129, v138, v139
	v_exp_f32_e32 v232, v92
	v_exp_f32_e32 v233, v93
	v_mfma_f32_32x32x16_bf16 v[48:63], a[228:231], a[132:135], v[48:63]
	ds_read_b64_tr_b16 v[190:191], v208 offset:0xe00
	v_cvt_pk_bf16_f32 v130, v140, v141
	v_mfma_f32_32x32x16_bf16 v[32:47], a[228:231], a[164:167], v[32:47]
	ds_read_b64_tr_b16 v[172:173], v208 offset:0x1000
	v_exp_f32_e32 v234, v94
	v_exp_f32_e32 v235, v95
	ds_read_b64_tr_b16 v[174:175], v208 offset:0x1800
	v_cvt_pk_bf16_f32 v131, v142, v143
	v_exp_f32_e32 v141, v64
	v_exp_f32_e32 v142, v65
	v_mfma_f32_32x32x16_bf16 v[112:127], a[200:203], a[136:139], v[112:127]
	ds_read_b64_tr_b16 v[168:169], v208 offset:0x1200
	v_cvt_pk_bf16_f32 v192, v144, v145
	v_exp_f32_e32 v143, v66
	v_mfma_f32_32x32x16_bf16 v[96:111], a[200:203], a[168:171], v[96:111]
	ds_read_b64_tr_b16 v[170:171], v208 offset:0x1a00
	v_exp_f32_e32 v244, v67
	v_cvt_pk_bf16_f32 v193, v146, v147
	v_mfma_f32_32x32x16_bf16 v[48:63], a[232:235], a[136:139], v[48:63]
	ds_read_b64_tr_b16 v[160:161], v208 offset:0x1400
	v_exp_f32_e32 v245, v68
	v_exp_f32_e32 v246, v69
	v_cvt_pk_bf16_f32 v194, v148, v149
	v_mfma_f32_32x32x16_bf16 v[32:47], a[232:235], a[168:171], v[32:47]
	ds_read_b64_tr_b16 v[162:163], v208 offset:0x1c00
	ds_read_b64_tr_b16 v[136:137], v208 offset:0x1600
	v_exp_f32_e32 v247, v70
	v_exp_f32_e32 v248, v71
	v_cvt_pk_bf16_f32 v195, v150, v151
	v_exp_f32_e32 v148, v72
	v_exp_f32_e32 v149, v73
	v_mfma_f32_32x32x16_bf16 v[112:127], a[204:207], a[140:143], v[112:127]
	ds_read_b64_tr_b16 v[138:139], v208 offset:0x1e00
	v_cvt_pk_bf16_f32 v144, v152, v153
	v_exp_f32_e32 v150, v74
	v_exp_f32_e32 v151, v75
	v_mfma_f32_32x32x16_bf16 v[96:111], a[204:207], a[172:175], v[96:111]
	ds_read_b64_tr_b16 v[132:133], v208 offset:0x2000
	v_cvt_pk_bf16_f32 v145, v154, v155
	v_exp_f32_e32 v152, v76
	v_exp_f32_e32 v153, v77
	v_mfma_f32_32x32x16_bf16 v[48:63], a[236:239], a[140:143], v[48:63]
	ds_read_b64_tr_b16 v[134:135], v208 offset:0x2800
	v_cvt_pk_bf16_f32 v146, v156, v157
	v_mfma_f32_32x32x16_bf16 v[32:47], a[236:239], a[172:175], v[32:47]
	ds_read_b64_tr_b16 v[92:93], v208 offset:0x2200
	v_exp_f32_e32 v154, v78
	v_exp_f32_e32 v155, v79
	ds_read_b64_tr_b16 v[94:95], v208 offset:0x2a00
	v_cvt_pk_bf16_f32 v147, v158, v159
	s_mov_b32 s0, s51
	v_mfma_f32_32x32x16_bf16 v[112:127], a[208:211], a[144:147], v[112:127]
	ds_read_b64_tr_b16 v[88:89], v208 offset:0x2400
	v_cvt_pk_bf16_f32 v84, v80, v81
	v_add_f32_e32 v64, v237, v80
	v_add_f32_e32 v65, v236, v81
	s_add_i32 s1, s17, 0xffffa000
	v_mfma_f32_32x32x16_bf16 v[96:111], a[208:211], a[176:179], v[96:111]
	ds_read_b64_tr_b16 v[90:91], v208 offset:0x2c00
	v_cvt_pk_bf16_f32 v85, v82, v83
	v_add_f32_e32 v64, v64, v82
	v_add_f32_e32 v65, v65, v83
	s_mov_b32 s81, s53
	v_mfma_f32_32x32x16_bf16 v[48:63], a[240:243], a[144:147], v[48:63]
	ds_read_b64_tr_b16 v[80:81], v208 offset:0x2600
	v_cvt_pk_bf16_f32 v86, v240, v241
	v_add_f32_e32 v64, v64, v240
	v_add_f32_e32 v65, v65, v241
	s_add_i32 s82, s17, 0xffffc000
	v_mfma_f32_32x32x16_bf16 v[32:47], a[240:243], a[176:179], v[32:47]
	ds_read_b64_tr_b16 v[82:83], v208 offset:0x2e00
	ds_read_b64_tr_b16 v[76:77], v208 offset:0x3000
	v_cvt_pk_bf16_f32 v87, v242, v243
	v_add_f32_e32 v64, v64, v242
	v_add_f32_e32 v65, v65, v243
	s_mov_b32 s83, s55
	v_mfma_f32_32x32x16_bf16 v[112:127], a[212:215], a[148:151], v[112:127]
	ds_read_b64_tr_b16 v[78:79], v208 offset:0x3800
	v_add_f32_e32 v64, v64, v198
	v_add_f32_e32 v65, v65, v199
	s_add_i32 s84, s17, 0xffffe000
	v_mfma_f32_32x32x16_bf16 v[96:111], a[212:215], a[180:183], v[96:111]
	ds_read_b64_tr_b16 v[72:73], v208 offset:0x3200
	v_add_f32_e32 v64, v64, v230
	v_add_f32_e32 v65, v65, v231
	s_mov_b32 s85, s57
	v_mfma_f32_32x32x16_bf16 v[48:63], a[244:247], a[148:151], v[48:63]
	ds_read_b64_tr_b16 v[74:75], v208 offset:0x3a00
	v_add_f32_e32 v64, v64, v232
	v_add_f32_e32 v65, v65, v233
	s_mov_b32 s86, s17
	v_mfma_f32_32x32x16_bf16 v[32:47], a[244:247], a[180:183], v[32:47]
	ds_read_b64_tr_b16 v[68:69], v208 offset:0x3400
	ds_read_b64_tr_b16 v[70:71], v208 offset:0x3c00
	v_add_f32_e32 v156, v64, v234
	v_add_f32_e32 v157, v65, v235
	s_mov_b32 s87, s31
	v_mfma_f32_32x32x16_bf16 v[112:127], a[216:219], a[152:155], v[112:127]
	ds_read_b64_tr_b16 v[64:65], v208 offset:0x3600
	v_cvt_pk_bf16_f32 v140, v141, v142
	v_add_f32_e32 v158, v238, v141
	v_add_f32_e32 v142, v239, v142
	v_mfma_f32_32x32x16_bf16 v[96:111], a[216:219], a[184:187], v[96:111]
	ds_read_b64_tr_b16 v[66:67], v208 offset:0x3e00
	v_cvt_pk_bf16_f32 v141, v143, v244
	v_add_f32_e32 v143, v158, v143
	v_add_f32_e32 v158, v142, v244
	v_mfma_f32_32x32x16_bf16 v[48:63], a[248:251], a[152:155], v[48:63]
	s_mov_b32 s88, s59
	v_cvt_pk_bf16_f32 v142, v245, v246
	v_add_f32_e32 v159, v143, v245
	v_add_f32_e32 v158, v158, v246
	v_mfma_f32_32x32x16_bf16 v[32:47], a[248:251], a[184:187], v[32:47]
	s_add_i32 s89, s17, 0xfffda080
	v_cvt_pk_bf16_f32 v143, v247, v248
	v_add_f32_e32 v159, v159, v247
	v_add_f32_e32 v158, v158, v248
	v_mfma_f32_32x32x16_bf16 v[112:127], a[220:223], a[156:159], v[112:127]
	s_mov_b32 s90, s61
	v_add_f32_e32 v159, v159, v148
	v_add_f32_e32 v158, v158, v149
	v_mfma_f32_32x32x16_bf16 v[96:111], a[220:223], a[188:191], v[96:111]
	v_add_f32_e32 v159, v159, v150
	v_add_f32_e32 v158, v158, v151
	v_mfma_f32_32x32x16_bf16 v[48:63], a[252:255], a[156:159], v[48:63]
	s_mov_b32 s91, s62
	v_add_f32_e32 v159, v159, v152
	v_add_f32_e32 v158, v158, v153
	v_mfma_f32_32x32x16_bf16 v[32:47], a[252:255], a[188:191], v[32:47]
	s_add_i32 s92, s17, 0xfffde080
	v_add_f32_e32 v159, v159, v154
	v_add_f32_e32 v158, v158, v155
	s_nop 4
	v_add_f32_e32 v156, v156, v157
	s_waitcnt vmcnt(0) lgkmcnt(0)
	s_barrier
	s_nop 0
	v_mov_b32_e32 v157, v156
	s_nop 1
	v_permlane32_swap_b32_e32 v156, v157
	v_add_f32_e32 v156, v156, v157
	v_add_f32_e32 v197, v197, v156
	v_add_f32_e32 v156, v159, v158
	v_mov_b32_e32 v157, v156
	s_nop 1
	v_permlane32_swap_b32_e32 v156, v157
	v_add_f32_e32 v156, v156, v157
	v_add_f32_e32 v196, v196, v156
	s_nop 1
	s_mov_b32 m0, s0
	v_mfma_f32_32x32x16_bf16 a[0:15], v[180:183], v[164:167], a[0:15]
	buffer_load_dwordx4 v209, s[4:7], s1 offen lds
	s_mov_b32 m0, s81
	v_mfma_f32_32x32x16_bf16 a[16:31], v[180:183], v[192:195], a[16:31]
	buffer_load_dwordx4 v210, s[4:7], s82 offen lds
	ds_read_b128 a[192:195], v204 offset:0
	s_mov_b32 m0, s83
	v_mfma_f32_32x32x16_bf16 a[32:47], v[184:187], v[164:167], a[32:47]
	buffer_load_dwordx4 v209, s[4:7], s84 offen lds
	ds_read_b128 a[196:199], v205 offset:0
	s_mov_b32 m0, s85
	v_mfma_f32_32x32x16_bf16 a[48:63], v[184:187], v[192:195], a[48:63]
	buffer_load_dwordx4 v210, s[4:7], s86 offen lds
	ds_read_b128 a[200:203], v206 offset:0
	s_mov_b32 m0, s87
	v_mfma_f32_32x32x16_bf16 a[64:79], v[176:179], v[164:167], a[64:79]
	buffer_load_dwordx4 v211, s[20:23], s19 offen lds
	ds_read_b128 a[204:207], v207 offset:0
	s_mov_b32 m0, s88
	v_mfma_f32_32x32x16_bf16 a[80:95], v[176:179], v[192:195], a[80:95]
	buffer_load_dwordx4 v211, s[20:23], s89 offen lds
	ds_read_b128 a[208:211], v204 offset:128
	s_mov_b32 m0, s90
	v_mfma_f32_32x32x16_bf16 a[96:111], v[188:191], v[164:167], a[96:111]
	buffer_load_dwordx4 v211, s[20:23], s24 offen lds
	ds_read_b128 a[212:215], v205 offset:128
	s_mov_b32 m0, s91
	v_mfma_f32_32x32x16_bf16 a[112:127], v[188:191], v[192:195], a[112:127]
	buffer_load_dwordx4 v211, s[20:23], s92 offen lds
	ds_read_b128 a[216:219], v206 offset:128
	v_mfma_f32_32x32x16_bf16 a[0:15], v[172:175], v[128:131], a[0:15]
	ds_read_b128 a[220:223], v207 offset:128
	v_max3_f32 v156, v112, v113, v48
	v_max3_f32 v157, v114, v115, v49
	v_max3_f32 v156, v156, v50, v51
	v_mfma_f32_32x32x16_bf16 a[16:31], v[172:175], v[144:147], a[16:31]
	ds_read_b128 a[224:227], v204 offset:8192
	v_max3_f32 v156, v156, v116, v117
	v_max3_f32 v157, v157, v118, v119
	v_max3_f32 v156, v156, v52, v53
	v_max3_f32 v157, v157, v54, v55
	v_mfma_f32_32x32x16_bf16 a[32:47], v[168:171], v[128:131], a[32:47]
	ds_read_b128 a[228:231], v205 offset:8192
	v_max3_f32 v156, v156, v120, v121
	v_max3_f32 v157, v157, v122, v123
	v_max3_f32 v156, v156, v56, v57
	v_max3_f32 v157, v157, v58, v59
	v_mfma_f32_32x32x16_bf16 a[48:63], v[168:171], v[144:147], a[48:63]
	ds_read_b128 a[232:235], v206 offset:8192
	v_max3_f32 v156, v156, v124, v125
	v_max3_f32 v157, v157, v126, v127
	v_max3_f32 v156, v156, v60, v61
	v_max3_f32 v157, v157, v62, v63
	v_mfma_f32_32x32x16_bf16 a[64:79], v[160:163], v[128:131], a[64:79]
	ds_read_b128 a[236:239], v207 offset:8192
	v_max3_f32 v158, v96, v97, v32
	v_max3_f32 v159, v98, v99, v33
	v_max3_f32 v158, v158, v34, v35
	v_mfma_f32_32x32x16_bf16 a[80:95], v[160:163], v[144:147], a[80:95]
	ds_read_b128 a[240:243], v204 offset:8320
	v_max3_f32 v158, v158, v100, v101
	v_max3_f32 v159, v159, v102, v103
	v_max3_f32 v158, v158, v36, v37
	v_max3_f32 v159, v159, v38, v39
	v_mfma_f32_32x32x16_bf16 a[96:111], v[136:139], v[128:131], a[96:111]
	ds_read_b128 a[244:247], v205 offset:8320
	v_max3_f32 v128, v158, v104, v105
	v_max3_f32 v129, v159, v106, v107
	v_max3_f32 v128, v128, v40, v41
	v_max3_f32 v129, v129, v42, v43
	v_mfma_f32_32x32x16_bf16 a[112:127], v[136:139], v[144:147], a[112:127]
	ds_read_b128 a[248:251], v206 offset:8320
	v_max3_f32 v128, v128, v108, v109
	v_max3_f32 v129, v129, v110, v111
	v_max3_f32 v128, v128, v44, v45
	v_max3_f32 v130, v129, v46, v47
	v_mfma_f32_32x32x16_bf16 a[0:15], v[132:135], v[84:87], a[0:15]
	ds_read_b128 a[252:255], v207 offset:8320
	v_max_f32_e32 v129, v156, v157
	v_mov_b32_e32 v131, v129
	s_nop 1
	v_permlane32_swap_b32_e32 v129, v131
	v_max_f32_e32 v129, v129, v131
	v_mfma_f32_32x32x16_bf16 a[16:31], v[132:135], v[140:143], a[16:31]
	v_max_f32_e32 v128, v128, v130
	v_mov_b32_e32 v130, v128
	s_nop 1
	v_permlane32_swap_b32_e32 v128, v130
	v_max_f32_e32 v128, v128, v130
	v_max_f32_e32 v130, v129, v129
	v_max_f32_e32 v131, v128, v128
	v_max_f32_e32 v130, v130, v131
	v_mfma_f32_32x32x16_bf16 a[32:47], v[92:95], v[84:87], a[32:47]
	v_cmp_lt_f32_e32 vcc, s79, v130
	s_cmp_lg_u64 vcc, 0
	s_cselect_b64 s[0:1], -1, 0
	s_cbranch_vccnz .LBB2_20
